# combo3 + hand-written P6 score epilogue: permlane32_swap pairs (m,m+1) so each dword store writes 2 keys x 128B full lines
# baseline (speedup 1.0000x reference)
.LBB0_690:
	s_lshl_b32 s15, s15, 9
	s_lshl_b32 s14, s14, 2
	s_add_i32 s15, s15, s31
	s_add_i32 s14, s15, s14
	v_mbcnt_lo_u32_b32 v160, -1, 0
	v_mbcnt_hi_u32_b32 v160, -1, v160
	v_lshrrev_b32_e32 v161, 5, v160
	v_mul_u32_u24_e32 v162, 0x7c0, v161
	v_sub_u32_e32 v162, 0, v162
	v_ashrrev_i32_e32 v163, 31, v162
	v_sub_u32_e32 v164, 1, v161
	v_mul_u32_u24_e32 v164, 0x7c0, v164
	v_mov_b32_e32 v165, 0
	s_add_i32 s24, s14, 0x0
	s_ashr_i32 s25, s24, 31
	s_lshl_b64 s[24:25], s[24:25], 15
	v_lshl_add_u64 v[166:167], v[132:133], 0, s[24:25]
	v_lshl_add_u64 v[168:169], v[166:167], 0, v[162:163]
	v_lshl_add_u64 v[170:171], v[166:167], 0, v[164:165]
	v_permlane32_swap_b32_e32 v124, v116
	v_permlane32_swap_b32_e32 v125, v117
	v_permlane32_swap_b32_e32 v126, v118
	v_permlane32_swap_b32_e32 v127, v119
	v_permlane32_swap_b32_e32 v108, v100
	v_permlane32_swap_b32_e32 v109, v101
	v_permlane32_swap_b32_e32 v110, v102
	v_permlane32_swap_b32_e32 v111, v103
	s_nop 1
	global_store_dword v[168:169], v124, off offset:0
	global_store_dword v[170:171], v116, off offset:64
	global_store_dword v[168:169], v125, off offset:256
	global_store_dword v[170:171], v117, off offset:320
	global_store_dword v[168:169], v126, off offset:512
	global_store_dword v[170:171], v118, off offset:576
	global_store_dword v[168:169], v127, off offset:768
	global_store_dword v[170:171], v119, off offset:832
	global_store_dword v[168:169], v108, off offset:128
	global_store_dword v[170:171], v100, off offset:192
	global_store_dword v[168:169], v109, off offset:384
	global_store_dword v[170:171], v101, off offset:448
	global_store_dword v[168:169], v110, off offset:640
	global_store_dword v[170:171], v102, off offset:704
	global_store_dword v[168:169], v111, off offset:896
	global_store_dword v[170:171], v103, off offset:960
	s_add_u32 s24, s24, 0x1000
	s_addc_u32 s25, s25, 0
	v_lshl_add_u64 v[166:167], v[132:133], 0, s[24:25]
	v_lshl_add_u64 v[168:169], v[166:167], 0, v[162:163]
	v_lshl_add_u64 v[170:171], v[166:167], 0, v[164:165]
	v_permlane32_swap_b32_e32 v120, v112
	v_permlane32_swap_b32_e32 v121, v113
	v_permlane32_swap_b32_e32 v122, v114
	v_permlane32_swap_b32_e32 v123, v115
	v_permlane32_swap_b32_e32 v104, v96
	v_permlane32_swap_b32_e32 v105, v97
	v_permlane32_swap_b32_e32 v106, v98
	v_permlane32_swap_b32_e32 v107, v99
	s_nop 1
	global_store_dword v[168:169], v120, off offset:0
	global_store_dword v[170:171], v112, off offset:64
	global_store_dword v[168:169], v121, off offset:256
	global_store_dword v[170:171], v113, off offset:320
	global_store_dword v[168:169], v122, off offset:512
	global_store_dword v[170:171], v114, off offset:576
	global_store_dword v[168:169], v123, off offset:768
	global_store_dword v[170:171], v115, off offset:832
	global_store_dword v[168:169], v104, off offset:128
	global_store_dword v[170:171], v96, off offset:192
	global_store_dword v[168:169], v105, off offset:384
	global_store_dword v[170:171], v97, off offset:448
	global_store_dword v[168:169], v106, off offset:640
	global_store_dword v[170:171], v98, off offset:704
	global_store_dword v[168:169], v107, off offset:896
	global_store_dword v[170:171], v99, off offset:960
	s_add_i32 s24, s14, 0x100
	s_ashr_i32 s25, s24, 31
	s_lshl_b64 s[24:25], s[24:25], 15
	v_lshl_add_u64 v[166:167], v[132:133], 0, s[24:25]
	v_lshl_add_u64 v[168:169], v[166:167], 0, v[162:163]
	v_lshl_add_u64 v[170:171], v[166:167], 0, v[164:165]
	v_permlane32_swap_b32_e32 v92, v84
	v_permlane32_swap_b32_e32 v93, v85
	v_permlane32_swap_b32_e32 v94, v86
	v_permlane32_swap_b32_e32 v95, v87
	v_permlane32_swap_b32_e32 v76, v68
	v_permlane32_swap_b32_e32 v77, v69
	v_permlane32_swap_b32_e32 v78, v70
	v_permlane32_swap_b32_e32 v79, v71
	s_nop 1
	global_store_dword v[168:169], v92, off offset:0
	global_store_dword v[170:171], v84, off offset:64
	global_store_dword v[168:169], v93, off offset:256
	global_store_dword v[170:171], v85, off offset:320
	global_store_dword v[168:169], v94, off offset:512
	global_store_dword v[170:171], v86, off offset:576
	global_store_dword v[168:169], v95, off offset:768
	global_store_dword v[170:171], v87, off offset:832
	global_store_dword v[168:169], v76, off offset:128
	global_store_dword v[170:171], v68, off offset:192
	global_store_dword v[168:169], v77, off offset:384
	global_store_dword v[170:171], v69, off offset:448
	global_store_dword v[168:169], v78, off offset:640
	global_store_dword v[170:171], v70, off offset:704
	global_store_dword v[168:169], v79, off offset:896
	global_store_dword v[170:171], v71, off offset:960
	s_add_u32 s24, s24, 0x1000
	s_addc_u32 s25, s25, 0
	v_lshl_add_u64 v[166:167], v[132:133], 0, s[24:25]
	v_lshl_add_u64 v[168:169], v[166:167], 0, v[162:163]
	v_lshl_add_u64 v[170:171], v[166:167], 0, v[164:165]
	v_permlane32_swap_b32_e32 v88, v80
	v_permlane32_swap_b32_e32 v89, v81
	v_permlane32_swap_b32_e32 v90, v82
	v_permlane32_swap_b32_e32 v91, v83
	v_permlane32_swap_b32_e32 v72, v64
	v_permlane32_swap_b32_e32 v73, v65
	v_permlane32_swap_b32_e32 v74, v66
	v_permlane32_swap_b32_e32 v75, v67
	s_nop 1
	global_store_dword v[168:169], v88, off offset:0
	global_store_dword v[170:171], v80, off offset:64
	global_store_dword v[168:169], v89, off offset:256
	global_store_dword v[170:171], v81, off offset:320
	global_store_dword v[168:169], v90, off offset:512
	global_store_dword v[170:171], v82, off offset:576
	global_store_dword v[168:169], v91, off offset:768
	global_store_dword v[170:171], v83, off offset:832
	global_store_dword v[168:169], v72, off offset:128
	global_store_dword v[170:171], v64, off offset:192
	global_store_dword v[168:169], v73, off offset:384
	global_store_dword v[170:171], v65, off offset:448
	global_store_dword v[168:169], v74, off offset:640
	global_store_dword v[170:171], v66, off offset:704
	global_store_dword v[168:169], v75, off offset:896
	global_store_dword v[170:171], v67, off offset:960
	s_add_i32 s24, s14, 0x2
	s_ashr_i32 s25, s24, 31
	s_lshl_b64 s[24:25], s[24:25], 15
	v_lshl_add_u64 v[166:167], v[132:133], 0, s[24:25]
	v_lshl_add_u64 v[168:169], v[166:167], 0, v[162:163]
	v_lshl_add_u64 v[170:171], v[166:167], 0, v[164:165]
	v_permlane32_swap_b32_e32 v60, v52
	v_permlane32_swap_b32_e32 v61, v53
	v_permlane32_swap_b32_e32 v62, v54
	v_permlane32_swap_b32_e32 v63, v55
	v_permlane32_swap_b32_e32 v44, v36
	v_permlane32_swap_b32_e32 v45, v37
	v_permlane32_swap_b32_e32 v46, v38
	v_permlane32_swap_b32_e32 v47, v39
	s_nop 1
	global_store_dword v[168:169], v60, off offset:0
	global_store_dword v[170:171], v52, off offset:64
	global_store_dword v[168:169], v61, off offset:256
	global_store_dword v[170:171], v53, off offset:320
	global_store_dword v[168:169], v62, off offset:512
	global_store_dword v[170:171], v54, off offset:576
	global_store_dword v[168:169], v63, off offset:768
	global_store_dword v[170:171], v55, off offset:832
	global_store_dword v[168:169], v44, off offset:128
	global_store_dword v[170:171], v36, off offset:192
	global_store_dword v[168:169], v45, off offset:384
	global_store_dword v[170:171], v37, off offset:448
	global_store_dword v[168:169], v46, off offset:640
	global_store_dword v[170:171], v38, off offset:704
	global_store_dword v[168:169], v47, off offset:896
	global_store_dword v[170:171], v39, off offset:960
	s_add_u32 s24, s24, 0x1000
	s_addc_u32 s25, s25, 0
	v_lshl_add_u64 v[166:167], v[132:133], 0, s[24:25]
	v_lshl_add_u64 v[168:169], v[166:167], 0, v[162:163]
	v_lshl_add_u64 v[170:171], v[166:167], 0, v[164:165]
	v_permlane32_swap_b32_e32 v56, v48
	v_permlane32_swap_b32_e32 v57, v49
	v_permlane32_swap_b32_e32 v58, v50
	v_permlane32_swap_b32_e32 v59, v51
	v_permlane32_swap_b32_e32 v40, v32
	v_permlane32_swap_b32_e32 v41, v33
	v_permlane32_swap_b32_e32 v42, v34
	v_permlane32_swap_b32_e32 v43, v35
	s_nop 1
	global_store_dword v[168:169], v56, off offset:0
	global_store_dword v[170:171], v48, off offset:64
	global_store_dword v[168:169], v57, off offset:256
	global_store_dword v[170:171], v49, off offset:320
	global_store_dword v[168:169], v58, off offset:512
	global_store_dword v[170:171], v50, off offset:576
	global_store_dword v[168:169], v59, off offset:768
	global_store_dword v[170:171], v51, off offset:832
	global_store_dword v[168:169], v40, off offset:128
	global_store_dword v[170:171], v32, off offset:192
	global_store_dword v[168:169], v41, off offset:384
	global_store_dword v[170:171], v33, off offset:448
	global_store_dword v[168:169], v42, off offset:640
	global_store_dword v[170:171], v34, off offset:704
	global_store_dword v[168:169], v43, off offset:896
	global_store_dword v[170:171], v35, off offset:960
	s_add_i32 s24, s14, 0x102
	s_ashr_i32 s25, s24, 31
	s_lshl_b64 s[24:25], s[24:25], 15
	v_lshl_add_u64 v[166:167], v[132:133], 0, s[24:25]
	v_lshl_add_u64 v[168:169], v[166:167], 0, v[162:163]
	v_lshl_add_u64 v[170:171], v[166:167], 0, v[164:165]
	v_permlane32_swap_b32_e32 v28, v20
	v_permlane32_swap_b32_e32 v29, v21
	v_permlane32_swap_b32_e32 v30, v22
	v_permlane32_swap_b32_e32 v31, v23
	v_permlane32_swap_b32_e32 v12, v4
	v_permlane32_swap_b32_e32 v13, v5
	v_permlane32_swap_b32_e32 v14, v6
	v_permlane32_swap_b32_e32 v15, v7
	s_nop 1
	global_store_dword v[168:169], v28, off offset:0
	global_store_dword v[170:171], v20, off offset:64
	global_store_dword v[168:169], v29, off offset:256
	global_store_dword v[170:171], v21, off offset:320
	global_store_dword v[168:169], v30, off offset:512
	global_store_dword v[170:171], v22, off offset:576
	global_store_dword v[168:169], v31, off offset:768
	global_store_dword v[170:171], v23, off offset:832
	global_store_dword v[168:169], v12, off offset:128
	global_store_dword v[170:171], v4, off offset:192
	global_store_dword v[168:169], v13, off offset:384
	global_store_dword v[170:171], v5, off offset:448
	global_store_dword v[168:169], v14, off offset:640
	global_store_dword v[170:171], v6, off offset:704
	global_store_dword v[168:169], v15, off offset:896
	global_store_dword v[170:171], v7, off offset:960
	s_add_u32 s24, s24, 0x1000
	s_addc_u32 s25, s25, 0
	v_lshl_add_u64 v[166:167], v[132:133], 0, s[24:25]
	v_lshl_add_u64 v[168:169], v[166:167], 0, v[162:163]
	v_lshl_add_u64 v[170:171], v[166:167], 0, v[164:165]
	v_permlane32_swap_b32_e32 v24, v16
	v_permlane32_swap_b32_e32 v25, v17
	v_permlane32_swap_b32_e32 v26, v18
	v_permlane32_swap_b32_e32 v27, v19
	v_permlane32_swap_b32_e32 v8, v0
	v_permlane32_swap_b32_e32 v9, v1
	v_permlane32_swap_b32_e32 v10, v2
	v_permlane32_swap_b32_e32 v11, v3
	s_nop 1
	global_store_dword v[168:169], v24, off offset:0
	global_store_dword v[170:171], v16, off offset:64
	global_store_dword v[168:169], v25, off offset:256
	global_store_dword v[170:171], v17, off offset:320
	global_store_dword v[168:169], v26, off offset:512
	global_store_dword v[170:171], v18, off offset:576
	global_store_dword v[168:169], v27, off offset:768
	global_store_dword v[170:171], v19, off offset:832
	global_store_dword v[168:169], v8, off offset:128
	global_store_dword v[170:171], v0, off offset:192
	global_store_dword v[168:169], v9, off offset:384
	global_store_dword v[170:171], v1, off offset:448
	global_store_dword v[168:169], v10, off offset:640
	global_store_dword v[170:171], v2, off offset:704
	global_store_dword v[168:169], v11, off offset:896
	global_store_dword v[170:171], v3, off offset:960
	s_andn2_b64 vcc, exec, s[4:5]
	s_mov_b64 s[4:5], -1
	s_cbranch_vccnz .LBB0_679
	s_andn2_b64 vcc, exec, s[8:9]
	s_cbranch_vccnz .LBB0_678
	s_barrier
	s_branch .LBB0_678
